# v066 + the last XCD leader no longer bumps (and waits on) the TOPGEN word at the 9 in-loop barrier sites, since leaders poll TOP there
# speedup vs baseline: 1.0022x; 1.0022x over previous
; __device__ __forceinline__ unsigned xb_ld(unsigned* p)              { return __hip_atomic_load(p, __ATOMIC_RELAXED, __HIP_MEMORY_SCOPE_AGENT); }
; __device__ __forceinline__ unsigned xb_add(unsigned* p, unsigned v) { return __hip_atomic_fetch_add(p, v, __ATOMIC_RELAXED, __HIP_MEMORY_SCOPE_AGENT); }
; #define XB_SPIN(cond, bar) do { unsigned _sp = 0; while (cond) { __builtin_amdgcn_s_sleep(1); \
;     if ((++_sp & 255u) == 0u) { if (xb_ld(&(bar)[XB_TMO])) break; if (_sp > XB_SPIN_CAP) { atomicAdd(&(bar)[XB_TMO], 1u); break; } } } } while (0)
; __device__ __forceinline__ void xcd_barrier(const XcdBarrier& b, const int tid) {
;     ...
;         const unsigned old = xb_add(&bar[XB_XSUB(b.x)], 1u);
;         const unsigned gen = old / nloc;
;         if (old + 1u == (gen + 1u) * nloc) {
;             __builtin_amdgcn_fence(__ATOMIC_RELEASE, "agent");
;             asm volatile("s_waitcnt vmcnt(0)" ::: "memory");
;             const unsigned og = xb_add(&bar[XB_TOP], 1u);
;             const unsigned tg = og / nx;
;             if (og + 1u == (tg + 1u) * nx) xb_add(&bar[XB_TOPGEN], 1u);
;             else XB_SPIN(xb_ld(&bar[XB_TOPGEN]) == tg, bar);
;             __builtin_amdgcn_fence(__ATOMIC_ACQUIRE, "agent");
.LBB0_747:
	s_or_b64 exec, exec, s[42:43]
	s_waitcnt vmcnt(0)
	v_readfirstlane_b32 s7, v3
	v_sub_u32_e32 v4, 0, v2
	v_readlane_b32 s22, v252, 15
	v_add_u32_e32 v3, s7, v0
	v_cvt_f32_u32_e32 v0, v2
	v_readlane_b32 s23, v252, 16
	s_mov_b64 s[42:43], 0
	v_rcp_iflag_f32_e32 v0, v0
	s_nop 0
	v_mul_f32_e32 v0, 0x4f7ffffe, v0
	v_cvt_u32_f32_e32 v0, v0
	v_mul_lo_u32 v4, v4, v0
	v_mul_hi_u32 v4, v0, v4
	v_add_u32_e32 v0, v0, v4
	v_mul_hi_u32 v0, v3, v0
	v_mul_lo_u32 v4, v0, v2
	v_sub_u32_e32 v4, v3, v4
	v_cmp_ge_u32_e32 vcc, v4, v2
	v_add_u32_e32 v5, 1, v0
	v_add_u32_e32 v3, 1, v3
	v_cndmask_b32_e32 v0, v0, v5, vcc
	v_sub_u32_e32 v5, v4, v2
	v_cndmask_b32_e32 v4, v4, v5, vcc
	v_cmp_ge_u32_e32 vcc, v4, v2
	v_add_u32_e32 v4, 1, v0
	s_nop 0
	v_cndmask_b32_e32 v0, v0, v4, vcc
	v_mul_lo_u32 v4, v2, v0
	v_add_u32_e32 v2, v4, v2
	v_cmp_ne_u32_e32 vcc, v3, v2
	v_mov_b32_e32 v5, v2
	v_mov_b64_e32 v[2:3], s[22:23]
	s_and_saveexec_b64 s[40:41], vcc
	s_cbranch_execz .LBB0_759
	v_readlane_b32 s22, v252, 13
	v_readlane_b32 s23, v252, 14
	s_mov_b64 s[44:45], 0
	s_nop 3
	global_load_dword v2, v1, s[22:23] sc1
	s_waitcnt vmcnt(0)
	v_cmp_lt_u32_e32 vcc, v2, v5
	s_and_saveexec_b64 s[42:43], vcc
	s_cbranch_execz .LBB0_758
	s_mov_b32 s7, 1
	s_branch .LBB0_751

; __device__ __forceinline__ unsigned xb_ld(unsigned* p)              { return __hip_atomic_load(p, __ATOMIC_RELAXED, __HIP_MEMORY_SCOPE_AGENT); }
; __device__ __forceinline__ unsigned xb_add(unsigned* p, unsigned v) { return __hip_atomic_fetch_add(p, v, __ATOMIC_RELAXED, __HIP_MEMORY_SCOPE_AGENT); }
; #define XB_SPIN(cond, bar) do { unsigned _sp = 0; while (cond) { __builtin_amdgcn_s_sleep(1); \
;     if ((++_sp & 255u) == 0u) { if (xb_ld(&(bar)[XB_TMO])) break; if (_sp > XB_SPIN_CAP) { atomicAdd(&(bar)[XB_TMO], 1u); break; } } } } while (0)
; __device__ __forceinline__ void xcd_barrier(const XcdBarrier& b, const int tid) {
;     ...
;         const unsigned old = xb_add(&bar[XB_XSUB(b.x)], 1u);
;         const unsigned gen = old / nloc;
;         if (old + 1u == (gen + 1u) * nloc) {
;             __builtin_amdgcn_fence(__ATOMIC_RELEASE, "agent");
;             asm volatile("s_waitcnt vmcnt(0)" ::: "memory");
;             const unsigned og = xb_add(&bar[XB_TOP], 1u);
;             const unsigned tg = og / nx;
;             if (og + 1u == (tg + 1u) * nx) xb_add(&bar[XB_TOPGEN], 1u);
;             else XB_SPIN(xb_ld(&bar[XB_TOPGEN]) == tg, bar);
;             __builtin_amdgcn_fence(__ATOMIC_ACQUIRE, "agent");
.LBB0_1819:
	s_or_b64 exec, exec, s[42:43]
	s_waitcnt vmcnt(0)
	v_readfirstlane_b32 s6, v3
	v_sub_u32_e32 v4, 0, v2
	s_mov_b64 s[42:43], 0
	v_add_u32_e32 v3, s6, v0
	v_cvt_f32_u32_e32 v0, v2
	v_readlane_b32 s6, v252, 15
	v_readlane_b32 s7, v252, 16
	v_rcp_iflag_f32_e32 v0, v0
	s_nop 0
	v_mul_f32_e32 v0, 0x4f7ffffe, v0
	v_cvt_u32_f32_e32 v0, v0
	v_mul_lo_u32 v4, v4, v0
	v_mul_hi_u32 v4, v0, v4
	v_add_u32_e32 v0, v0, v4
	v_mul_hi_u32 v0, v3, v0
	v_mul_lo_u32 v4, v0, v2
	v_sub_u32_e32 v4, v3, v4
	v_cmp_ge_u32_e32 vcc, v4, v2
	v_add_u32_e32 v5, 1, v0
	v_add_u32_e32 v3, 1, v3
	v_cndmask_b32_e32 v0, v0, v5, vcc
	v_sub_u32_e32 v5, v4, v2
	v_cndmask_b32_e32 v4, v4, v5, vcc
	v_cmp_ge_u32_e32 vcc, v4, v2
	v_add_u32_e32 v4, 1, v0
	s_nop 0
	v_cndmask_b32_e32 v0, v0, v4, vcc
	v_mul_lo_u32 v4, v2, v0
	v_add_u32_e32 v2, v4, v2
	v_cmp_ne_u32_e32 vcc, v3, v2
	v_mov_b32_e32 v5, v2
	v_mov_b64_e32 v[2:3], s[6:7]
	s_and_saveexec_b64 s[40:41], vcc
	s_cbranch_execz .LBB0_1831
	v_readlane_b32 s6, v252, 13
	v_readlane_b32 s7, v252, 14
	s_mov_b64 s[44:45], 0
	s_nop 3
	global_load_dword v2, v1, s[6:7] sc1
	s_waitcnt vmcnt(0)
	v_cmp_lt_u32_e32 vcc, v2, v5
	s_and_saveexec_b64 s[42:43], vcc
	s_cbranch_execz .LBB0_1830
	s_mov_b32 s6, 1
	s_branch .LBB0_1823
